# attention: skip the sliding-window mask on band tiles where this wave's queries cannot reach the window edge (wave-uniform test), on top of in-register reductions
# baseline (speedup 1.0000x reference)
; #define LAS __attribute__((address_space(3)))
; __device__ __forceinline__ void phase_attention(const Frame& F, const Args& a) {
;     ...
;             const bool isctx = ti >= nband; const int kt = isctx ? (ti - nband) : (kt_lo + ti);
;             const LAS bf16_t* Ks = (const LAS bf16_t*)(F.lds + (step & 1) * ABUF); const LAS bf16_t* Vs = (const LAS bf16_t*)(F.lds + (step & 1) * ABUF + 17408);
;             f32x4 s[2][4];
; #pragma unroll
;             for (int m = 0; m < 2; ++m)
; #pragma unroll
;                 for (int nn = 0; nn < 4; ++nn) s[m][nn] = (f32x4){0.f, 0.f, 0.f, 0.f};
;             __builtin_amdgcn_s_setprio(1);
; #pragma unroll
;             for (int kk = 0; kk < 4; ++kk)
; #pragma unroll
;                 for (int nn = 0; nn < 4; ++nn) { const bf16x8 kf = *(const LAS bf16x8*)(Ks + (16 * nn + fr) * 136 + 32 * kk + 8 * fq);
; #pragma unroll
;                     for (int m = 0; m < 2; ++m) s[m][nn] = __builtin_amdgcn_mfma_f32_16x16x32_bf16(kf, aq[m][kk], s[m][nn], 0, 0, 0); }
;             __builtin_amdgcn_s_setprio(0);
;             bf16x8 pf[2][2];
; #pragma unroll
;             for (int m = 0; m < 2; ++m) {
;                 if (!isctx) { const int qpos = qpos0 + 16 * m + fr;
; #pragma unroll
;                     for (int nn = 0; nn < 4; ++nn)
; #pragma unroll
;                         for (int j = 0; j < 4; ++j) { const int d = 64 * kt + 16 * nn + 4 * fq + j - qpos; if (d > 128 || d < -128) s[m][nn][j] = -INFINITY; } }
.LBB0_2782:
	s_cmp_le_i32 s0, s27
	s_cselect_b64 s[16:17], -1, 0
	s_cmp_gt_i32 s0, s27
	s_cselect_b64 s[0:1], -1, 0
	s_and_b64 vcc, s[0:1], exec
	s_cselect_b32 s0, s28, s2
	s_bitcmp1_b32 s42, 0
	s_cselect_b32 s1, 0x8c00, 0
	s_add_i32 s0, s0, s42
	s_add_i32 s44, s1, 0
	s_add_i32 s0, s0, s43
	s_setprio 1
	v_add3_u32 v3, s44, v155, v175
	ds_read_b128 v[118:121], v3
	ds_read_b128 v[122:125], v3 offset:64
	ds_read_b128 v[130:133], v3 offset:4352
	ds_read_b128 v[134:137], v3 offset:4416
	ds_read_b128 v[142:145], v3 offset:8704
	ds_read_b128 v[146:149], v3 offset:8768
	ds_read_b128 v[194:197], v3 offset:13056
	ds_read_b128 v[198:201], v3 offset:13120
	s_waitcnt lgkmcnt(7)
	v_mfma_f32_16x16x32_bf16 v[126:129], v[118:121], v[18:21], 0
	v_mfma_f32_16x16x32_bf16 v[118:121], v[118:121], v[22:25], 0
	s_waitcnt lgkmcnt(5)
	v_mfma_f32_16x16x32_bf16 v[138:141], v[130:133], v[18:21], 0
	v_mfma_f32_16x16x32_bf16 v[130:133], v[130:133], v[22:25], 0
	s_waitcnt lgkmcnt(3)
	v_mfma_f32_16x16x32_bf16 v[190:193], v[142:145], v[18:21], 0
	v_mfma_f32_16x16x32_bf16 v[142:145], v[142:145], v[22:25], 0
	s_waitcnt lgkmcnt(1)
	v_mfma_f32_16x16x32_bf16 v[204:207], v[194:197], v[18:21], 0
	v_mfma_f32_16x16x32_bf16 v[194:197], v[194:197], v[22:25], 0
	v_mfma_f32_16x16x32_bf16 v[126:129], v[122:125], v[14:17], v[126:129]
	v_mfma_f32_16x16x32_bf16 v[118:121], v[122:125], v[26:29], v[118:121]
	v_mfma_f32_16x16x32_bf16 v[122:125], v[134:137], v[14:17], v[138:141]
	v_mfma_f32_16x16x32_bf16 v[130:133], v[134:137], v[26:29], v[130:133]
	v_mfma_f32_16x16x32_bf16 v[134:137], v[146:149], v[14:17], v[190:193]
	v_mfma_f32_16x16x32_bf16 v[138:141], v[146:149], v[26:29], v[142:145]
	s_waitcnt lgkmcnt(0)
	v_mfma_f32_16x16x32_bf16 v[146:149], v[198:201], v[26:29], v[194:197]
	ds_read_b128 v[190:193], v3 offset:128
	s_nop 1
	ds_read_b128 v[194:197], v3 offset:192
	v_mfma_f32_16x16x32_bf16 v[142:145], v[198:201], v[14:17], v[204:207]
	s_waitcnt lgkmcnt(1)
	v_mfma_f32_16x16x32_bf16 v[126:129], v[190:193], v[10:13], v[126:129]
	s_waitcnt vmcnt(1)
	v_mfma_f32_16x16x32_bf16 v[118:121], v[190:193], v[30:33], v[118:121]
	ds_read_b128 v[190:193], v3 offset:4480
	ds_read_b128 v[198:201], v3 offset:4544
	s_waitcnt lgkmcnt(1)
	v_mfma_f32_16x16x32_bf16 v[122:125], v[190:193], v[10:13], v[122:125]
	v_mfma_f32_16x16x32_bf16 v[130:133], v[190:193], v[30:33], v[130:133]
	ds_read_b128 v[190:193], v3 offset:8832
	ds_read_b128 v[204:207], v3 offset:8896
	s_waitcnt lgkmcnt(1)
	v_mfma_f32_16x16x32_bf16 v[208:211], v[190:193], v[10:13], v[134:137]
	s_nop 2
	ds_read_b128 v[134:137], v3 offset:13184
	ds_read_b128 v[212:215], v3 offset:13248
	v_mfma_f32_16x16x32_bf16 v[190:193], v[190:193], v[30:33], v[138:141]
	s_waitcnt lgkmcnt(1)
	v_mfma_f32_16x16x32_bf16 v[216:219], v[134:137], v[10:13], v[142:145]
	v_mfma_f32_16x16x32_bf16 v[220:223], v[134:137], v[30:33], v[146:149]
	v_mfma_f32_16x16x32_bf16 v[146:149], v[194:197], v[6:9], v[126:129]
	s_waitcnt vmcnt(0)
	v_mfma_f32_16x16x32_bf16 v[138:141], v[194:197], v[34:37], v[118:121]
	v_mfma_f32_16x16x32_bf16 v[142:145], v[198:201], v[6:9], v[122:125]
	v_mfma_f32_16x16x32_bf16 v[134:137], v[198:201], v[34:37], v[130:133]
	v_mfma_f32_16x16x32_bf16 v[126:129], v[204:207], v[6:9], v[208:211]
	v_mfma_f32_16x16x32_bf16 v[130:133], v[204:207], v[34:37], v[190:193]
	s_waitcnt lgkmcnt(0)
	v_mfma_f32_16x16x32_bf16 v[118:121], v[212:215], v[6:9], v[216:219]
	v_mfma_f32_16x16x32_bf16 v[122:125], v[212:215], v[34:37], v[220:223]
	s_setprio 0
	s_lshl_b32 s99, s0, 6
	s_sub_i32 s99, s99, s41
	s_addk_i32 s99, 0x61
	s_cmp_le_u32 s99, 0xa2
	s_cselect_b64 s[98:99], -1, 0
	s_or_b64 vcc, vcc, s[98:99]
	s_andn2_b64 s[16:17], s[16:17], s[98:99]
	v_lshl_add_u32 v3, s0, 6, v181
	v_subrev_u32_e32 v199, s41, v3
	v_cmp_gt_u32_e64 s[0:1], s22, v199
	v_add_u32_e32 v200, 1, v199
	v_add_u32_e32 v198, 2, v199
	v_add_u32_e32 v197, 3, v199
	v_add_u32_e32 v196, 16, v199
	v_add_u32_e32 v195, 17, v199
	v_add_u32_e32 v194, 18, v199
	v_add_u32_e32 v193, 19, v199
	v_add_u32_e32 v192, 32, v199
	v_add_u32_e32 v191, 33, v199
	v_add_u32_e32 v190, 34, v199
	v_add_u32_e32 v5, 35, v199
	s_cbranch_vccnz .LBB0_2784
	v_cmp_lt_u32_e32 vcc, s24, v200
	v_mov_b32_e32 v204, s23
	v_add_u32_e32 v3, 48, v199
	v_cndmask_b32_e32 v147, v183, v147, vcc
	v_cmp_lt_u32_e32 vcc, s24, v198
	v_cndmask_b32_e64 v146, v146, v204, s[0:1]
	s_nop 0
	v_cndmask_b32_e32 v148, v183, v148, vcc
	v_cmp_lt_u32_e32 vcc, s24, v197
	s_nop 1
	v_cndmask_b32_e32 v149, v183, v149, vcc
	v_cmp_gt_u32_e32 vcc, s22, v196
	s_nop 1
	v_cndmask_b32_e32 v142, v142, v204, vcc
	v_cmp_lt_u32_e32 vcc, s24, v195
	s_nop 1
	v_cndmask_b32_e32 v143, v183, v143, vcc
	v_cmp_lt_u32_e32 vcc, s24, v194
	s_nop 1
	v_cndmask_b32_e32 v144, v183, v144, vcc
	v_cmp_lt_u32_e32 vcc, s24, v193
	s_nop 1
	v_cndmask_b32_e32 v145, v183, v145, vcc
	v_cmp_gt_u32_e32 vcc, s22, v192
	s_nop 1
	v_cndmask_b32_e32 v126, v126, v204, vcc
	v_cmp_lt_u32_e32 vcc, s24, v191
	s_nop 1
	v_cndmask_b32_e32 v127, v183, v127, vcc
	v_cmp_lt_u32_e32 vcc, s24, v190
	s_nop 1
	v_cndmask_b32_e32 v128, v183, v128, vcc
	v_cmp_lt_u32_e32 vcc, s24, v5
	s_nop 1
	v_cndmask_b32_e32 v129, v183, v129, vcc
	v_cmp_gt_u32_e32 vcc, s22, v3
	v_add_u32_e32 v3, 49, v199
	s_nop 0
	v_cndmask_b32_e32 v118, v118, v204, vcc
	v_cmp_lt_u32_e32 vcc, s24, v3
	v_add_u32_e32 v3, 50, v199
	s_nop 0
	v_cndmask_b32_e32 v119, v183, v119, vcc
	v_cmp_lt_u32_e32 vcc, s24, v3
	v_add_u32_e32 v3, 51, v199
	s_nop 0
	v_cndmask_b32_e32 v120, v183, v120, vcc
	v_cmp_lt_u32_e32 vcc, s24, v3
	s_nop 1
	v_cndmask_b32_e32 v121, v183, v121, vcc
